# MoE GEMM unit-loop header (next-unit lookup) rewritten: geo table read once into lanes, expert by compare+bcnt, rowtab reads issued together: one LDS round trip instead of four
# speedup vs baseline: 1.0200x; 1.0069x over previous
.LBB0_1639:
	v_and_b32_e32 v2, 63, v0
	s_add_i32 s50, s18, 1
	v_min_u32_e32 v2, 16, v2
	s_lshl_b32 s15, s50, 10
	v_lshlrev_b32_e32 v2, 2, v2
	s_add_i32 s20, s15, 0x20400
	v_add_u32_e32 v2, 0x20010, v2
	s_add_i32 s21, s15, 0x20600
	ds_read_b32 v3, v2
	v_add_u32_e32 v5, s20, v213
	v_add_u32_e32 v6, s20, v214
	v_add_u32_e32 v7, s21, v213
	v_add_u32_e32 v8, s21, v214
	ds_read_b32 v5, v5
	ds_read_b32 v6, v6
	ds_read_b32 v7, v7
	ds_read_b32 v8, v8
	v_readlane_b32 s1, v243, 52
	v_readlane_b32 s19, v243, 0
	s_mul_i32 s0, s50, s49
	s_nop 0
	s_add_i32 s0, s0, s1
	s_lshr_b32 s20, s0, 3
	s_and_b32 s14, s0, 7
	s_waitcnt lgkmcnt(0)
	v_readlane_b32 s15, v3, 16
	s_nop 3
	s_add_i32 s1, s15, 7
	s_ashr_i32 s1, s1, 3
	s_mul_i32 s19, s1, s19
	s_add_i32 s51, s19, s20
	s_cmp_lt_i32 s20, s1
	s_cselect_b32 s15, s15, 0
	s_cmp_lt_i32 s51, s15
	s_cselect_b64 s[0:1], 0, -1
	s_cbranch_scc0 .LBB0_1641
	v_cmp_ge_i32_e32 vcc, s51, v3
	v_add_u32_e32 v219, v6, v211
	v_add_u32_e32 v221, v7, v1
	v_add_u32_e32 v222, v8, v211
	v_add_u32_e32 v220, v5, v1
	s_and_b32 s19, vcc_lo, 0xfffe
	s_bcnt1_i32_b32 s19, s19
	s_mov_b32 s15, 0
	s_lshl_b64 s[16:17], s[14:15], 18
	s_lshl_b32 s20, s19, 21
	s_add_u32 s16, s16, s20
	s_addc_u32 s17, s17, 0
	s_add_u32 s16, s16, s6
	s_addc_u32 s17, s17, s7

.LBB0_1794:
	v_and_b32_e32 v2, 63, v0
	s_add_i32 s50, s52, 1
	v_min_u32_e32 v2, 16, v2
	v_readlane_b32 s1, v243, 52
	v_lshlrev_b32_e32 v2, 2, v2
	v_readlane_b32 s19, v243, 0
	v_add_u32_e32 v2, 0x20010, v2
	s_mul_i32 s0, s50, s49
	ds_read_b32 v3, v2
	s_add_i32 s0, s0, s1
	s_lshr_b32 s20, s0, 2
	s_and_b32 s14, s0, 3
	s_waitcnt lgkmcnt(0)
	v_readlane_b32 s18, v3, 16
	s_nop 3
	s_add_i32 s1, s18, 7
	s_ashr_i32 s1, s1, 3
	s_mul_i32 s19, s1, s19
	s_add_i32 s15, s19, s20
	s_cmp_lt_i32 s20, s1
	s_cselect_b32 s18, s18, 0
	s_cmp_lt_i32 s15, s18
	s_cselect_b64 s[0:1], 0, -1
	s_cbranch_scc0 .LBB0_1796
	v_cmp_ge_i32_e32 vcc, s15, v3
	s_lshl_b32 s18, s15, 8
	v_add_u32_e32 v4, s18, v212
	v_add_u32_e32 v5, s18, v1
	s_bitset1_b32 s18, 7
	v_lshl_add_u32 v219, v4, 10, v213
	v_add_u32_e32 v4, s18, v1
	v_lshl_add_u32 v220, v4, 10, v210
	v_add_u32_e32 v4, s18, v212
	v_lshl_add_u32 v221, v5, 10, v210
	v_lshl_add_u32 v222, v4, 10, v213
	s_and_b32 s19, vcc_lo, 0xfffe
	s_bcnt1_i32_b32 s19, s19
	s_mov_b32 s15, 0
	s_lshl_b64 s[16:17], s[14:15], 18
	s_lshl_b32 s20, s19, 20
	s_add_u32 s16, s16, s20
	s_addc_u32 s17, s17, 0
	s_add_u32 s16, s16, s6
	s_addc_u32 s17, s17, s7
